# grid barrier release path rewritten: every XCD leader adds to all per-XCD release words after its write-back (no top-level counter round trip), L1 invalidate at arrival
# speedup vs baseline: 1.0352x; 1.0051x over previous
.LBB0_70:
	v_readlane_b32 s2, v253, 36
	s_lshl_b32 s2, s2, 8
	v_readlane_b32 s4, v253, 34
	v_readlane_b32 s5, v253, 35
	s_add_u32 s2, s4, s2
	s_addc_u32 s3, s5, 0
	v_mov_b32_e32 v2, 0x1000
	v_mov_b32_e32 v4, 1
	global_atomic_add v4, v2, v4, s[2:3] offset:1024 sc0
	v_cvt_f32_u32_e32 v2, v3
	v_sub_u32_e32 v5, 0, v3
	v_rcp_iflag_f32_e32 v2, v2
	s_nop 0
	v_mul_f32_e32 v2, 0x4f7ffffe, v2
	v_cvt_u32_f32_e32 v2, v2
	v_mul_lo_u32 v5, v5, v2
	v_mul_hi_u32 v5, v2, v5
	v_add_u32_e32 v2, v2, v5
	s_waitcnt vmcnt(0)
	v_mul_hi_u32 v2, v4, v2
	v_mul_lo_u32 v5, v2, v3
	v_sub_u32_e32 v5, v4, v5
	v_add_u32_e32 v6, 1, v2
	v_cmp_ge_u32_e32 vcc, v5, v3
	v_add_u32_e32 v4, 1, v4
	s_nop 0
	v_cndmask_b32_e32 v2, v2, v6, vcc
	v_sub_u32_e32 v6, v5, v3
	v_cndmask_b32_e32 v5, v5, v6, vcc
	v_add_u32_e32 v6, 1, v2
	v_cmp_ge_u32_e32 vcc, v5, v3
	s_nop 1
	v_cndmask_b32_e32 v2, v2, v6, vcc
	v_mul_lo_u32 v5, v3, v2
	v_add_u32_e32 v3, v5, v3
	v_cmp_ne_u32_e32 vcc, v4, v3
	s_and_saveexec_b64 s[4:5], vcc
	s_xor_b64 s[4:5], exec, s[4:5]
	s_cbranch_execz .LBB0_84
	s_waitcnt lgkmcnt(0)
	buffer_inv sc1
	v_mad_u32_u24 v3, v2, v1, v1
	v_mov_b32_e32 v4, 0x2000
	s_mov_b32 s26, 0
.Lxbn_0:
	global_load_dword v5, v4, s[2:3] offset:1024 sc1
	s_waitcnt vmcnt(0)
	v_sub_u32_e32 v5, v5, v3
	v_cmp_gt_i32_e32 vcc, 0, v5
	s_cbranch_vccz .Lxbnd_0
	s_sleep 1
	s_add_u32 s26, s26, 1
	s_cmp_lt_u32 s26, 0x100000
	s_cbranch_scc1 .Lxbn_0

.LBB0_84:
	s_andn2_saveexec_b64 s[4:5], s[4:5]
	s_cbranch_execz .LBB0_102
	buffer_wbl2 sc1
	s_waitcnt vmcnt(0) lgkmcnt(0)
	v_mad_u32_u24 v3, v2, v1, v1
	v_mov_b32_e32 v4, 0x6400
	v_mov_b32_e32 v6, 1
	global_atomic_add v4, v6, s[48:49]
	v_add_u32_e32 v4, 0x100, v4
	global_atomic_add v4, v6, s[48:49]
	v_add_u32_e32 v4, 0x100, v4
	global_atomic_add v4, v6, s[48:49]
	v_add_u32_e32 v4, 0x100, v4
	global_atomic_add v4, v6, s[48:49]
	v_add_u32_e32 v4, 0x100, v4
	global_atomic_add v4, v6, s[48:49]
	v_add_u32_e32 v4, 0x100, v4
	global_atomic_add v4, v6, s[48:49]
	v_add_u32_e32 v4, 0x100, v4
	global_atomic_add v4, v6, s[48:49]
	v_add_u32_e32 v4, 0x100, v4
	global_atomic_add v4, v6, s[48:49]
	v_add_u32_e32 v4, 0x100, v4
	global_atomic_add v4, v6, s[48:49]
	v_add_u32_e32 v4, 0x100, v4
	global_atomic_add v4, v6, s[48:49]
	v_add_u32_e32 v4, 0x100, v4
	global_atomic_add v4, v6, s[48:49]
	v_add_u32_e32 v4, 0x100, v4
	global_atomic_add v4, v6, s[48:49]
	v_add_u32_e32 v4, 0x100, v4
	global_atomic_add v4, v6, s[48:49]
	v_add_u32_e32 v4, 0x100, v4
	global_atomic_add v4, v6, s[48:49]
	v_add_u32_e32 v4, 0x100, v4
	global_atomic_add v4, v6, s[48:49]
	v_add_u32_e32 v4, 0x100, v4
	global_atomic_add v4, v6, s[48:49]
	buffer_inv sc1
	v_mov_b32_e32 v4, 0x2000
	s_mov_b32 s26, 0

.Lxbld_0:
	s_waitcnt vmcnt(0)
.LBB0_102:
	s_or_b64 exec, exec, s[0:1]
	s_waitcnt lgkmcnt(0)
	s_barrier

.LBB0_575:
	v_readlane_b32 s2, v253, 36
	s_lshl_b32 s2, s2, 8
	v_readlane_b32 s4, v253, 34
	v_readlane_b32 s5, v253, 35
	s_add_u32 s2, s4, s2
	s_addc_u32 s3, s5, 0
	v_mov_b32_e32 v2, 0x1000
	v_mov_b32_e32 v4, 1
	global_atomic_add v4, v2, v4, s[2:3] offset:1024 sc0
	v_cvt_f32_u32_e32 v2, v3
	v_sub_u32_e32 v5, 0, v3
	v_rcp_iflag_f32_e32 v2, v2
	s_nop 0
	v_mul_f32_e32 v2, 0x4f7ffffe, v2
	v_cvt_u32_f32_e32 v2, v2
	v_mul_lo_u32 v5, v5, v2
	v_mul_hi_u32 v5, v2, v5
	v_add_u32_e32 v2, v2, v5
	s_waitcnt vmcnt(0)
	v_mul_hi_u32 v2, v4, v2
	v_mul_lo_u32 v5, v2, v3
	v_sub_u32_e32 v5, v4, v5
	v_add_u32_e32 v6, 1, v2
	v_cmp_ge_u32_e32 vcc, v5, v3
	v_add_u32_e32 v4, 1, v4
	s_nop 0
	v_cndmask_b32_e32 v2, v2, v6, vcc
	v_sub_u32_e32 v6, v5, v3
	v_cndmask_b32_e32 v5, v5, v6, vcc
	v_add_u32_e32 v6, 1, v2
	v_cmp_ge_u32_e32 vcc, v5, v3
	s_nop 1
	v_cndmask_b32_e32 v2, v2, v6, vcc
	v_mul_lo_u32 v5, v3, v2
	v_add_u32_e32 v3, v5, v3
	v_cmp_ne_u32_e32 vcc, v4, v3
	s_and_saveexec_b64 s[4:5], vcc
	s_xor_b64 s[4:5], exec, s[4:5]
	s_cbranch_execz .LBB0_589
	s_waitcnt lgkmcnt(0)
	buffer_inv sc1
	v_mad_u32_u24 v3, v2, v1, v1
	v_mov_b32_e32 v4, 0x2000
	s_mov_b32 s22, 0
.Lxbn_1:
	global_load_dword v5, v4, s[2:3] offset:1024 sc1
	s_waitcnt vmcnt(0)
	v_sub_u32_e32 v5, v5, v3
	v_cmp_gt_i32_e32 vcc, 0, v5
	s_cbranch_vccz .Lxbnd_1
	s_sleep 1
	s_add_u32 s22, s22, 1
	s_cmp_lt_u32 s22, 0x100000
	s_cbranch_scc1 .Lxbn_1

.LBB0_589:
	s_andn2_saveexec_b64 s[4:5], s[4:5]
	s_cbranch_execz .LBB0_607
	buffer_wbl2 sc1
	s_waitcnt vmcnt(0) lgkmcnt(0)
	v_mad_u32_u24 v3, v2, v1, v1
	v_mov_b32_e32 v4, 0x6400
	v_mov_b32_e32 v6, 1
	global_atomic_add v4, v6, s[48:49]
	v_add_u32_e32 v4, 0x100, v4
	global_atomic_add v4, v6, s[48:49]
	v_add_u32_e32 v4, 0x100, v4
	global_atomic_add v4, v6, s[48:49]
	v_add_u32_e32 v4, 0x100, v4
	global_atomic_add v4, v6, s[48:49]
	v_add_u32_e32 v4, 0x100, v4
	global_atomic_add v4, v6, s[48:49]
	v_add_u32_e32 v4, 0x100, v4
	global_atomic_add v4, v6, s[48:49]
	v_add_u32_e32 v4, 0x100, v4
	global_atomic_add v4, v6, s[48:49]
	v_add_u32_e32 v4, 0x100, v4
	global_atomic_add v4, v6, s[48:49]
	v_add_u32_e32 v4, 0x100, v4
	global_atomic_add v4, v6, s[48:49]
	v_add_u32_e32 v4, 0x100, v4
	global_atomic_add v4, v6, s[48:49]
	v_add_u32_e32 v4, 0x100, v4
	global_atomic_add v4, v6, s[48:49]
	v_add_u32_e32 v4, 0x100, v4
	global_atomic_add v4, v6, s[48:49]
	v_add_u32_e32 v4, 0x100, v4
	global_atomic_add v4, v6, s[48:49]
	v_add_u32_e32 v4, 0x100, v4
	global_atomic_add v4, v6, s[48:49]
	v_add_u32_e32 v4, 0x100, v4
	global_atomic_add v4, v6, s[48:49]
	v_add_u32_e32 v4, 0x100, v4
	global_atomic_add v4, v6, s[48:49]
	buffer_inv sc1
	v_mov_b32_e32 v4, 0x2000
	s_mov_b32 s22, 0

.Lxbld_1:
	s_waitcnt vmcnt(0)
.LBB0_607:
	s_or_b64 exec, exec, s[0:1]
	s_waitcnt lgkmcnt(0)
	s_barrier

.Lxbld_2:
	s_waitcnt vmcnt(0)
.LBB0_697:
	s_or_b64 exec, exec, s[0:1]
	s_waitcnt lgkmcnt(0)
	s_barrier

.Lxbld_3:
	s_waitcnt vmcnt(0)
.LBB0_752:
	s_or_b64 exec, exec, s[0:1]
	s_waitcnt lgkmcnt(0)
	s_barrier

.Lxbld_4:
	s_waitcnt vmcnt(0)
.LBB0_846:
	s_or_b64 exec, exec, s[0:1]
	s_waitcnt lgkmcnt(0)
	s_barrier

.Lxbld_5:
	s_waitcnt vmcnt(0)
.LBB0_914:
	s_or_b64 exec, exec, s[0:1]
	s_waitcnt lgkmcnt(0)
	s_barrier

.LBB0_959:
	v_readlane_b32 s4, v253, 36
	s_lshl_b32 s4, s4, 8
	v_readlane_b32 s6, v253, 34
	v_readlane_b32 s7, v253, 35
	s_add_u32 s4, s6, s4
	s_addc_u32 s5, s7, 0
	v_mov_b32_e32 v2, 0x1000
	v_mov_b32_e32 v4, 1
	global_atomic_add v4, v2, v4, s[4:5] offset:1024 sc0
	v_cvt_f32_u32_e32 v2, v3
	v_sub_u32_e32 v5, 0, v3
	v_rcp_iflag_f32_e32 v2, v2
	s_nop 0
	v_mul_f32_e32 v2, 0x4f7ffffe, v2
	v_cvt_u32_f32_e32 v2, v2
	v_mul_lo_u32 v5, v5, v2
	v_mul_hi_u32 v5, v2, v5
	v_add_u32_e32 v2, v2, v5
	s_waitcnt vmcnt(0)
	v_mul_hi_u32 v2, v4, v2
	v_mul_lo_u32 v5, v2, v3
	v_sub_u32_e32 v5, v4, v5
	v_add_u32_e32 v6, 1, v2
	v_cmp_ge_u32_e32 vcc, v5, v3
	v_add_u32_e32 v4, 1, v4
	s_nop 0
	v_cndmask_b32_e32 v2, v2, v6, vcc
	v_sub_u32_e32 v6, v5, v3
	v_cndmask_b32_e32 v5, v5, v6, vcc
	v_add_u32_e32 v6, 1, v2
	v_cmp_ge_u32_e32 vcc, v5, v3
	s_nop 1
	v_cndmask_b32_e32 v2, v2, v6, vcc
	v_mul_lo_u32 v5, v3, v2
	v_add_u32_e32 v3, v5, v3
	v_cmp_ne_u32_e32 vcc, v4, v3
	s_and_saveexec_b64 s[6:7], vcc
	s_xor_b64 s[6:7], exec, s[6:7]
	s_cbranch_execz .LBB0_973
	s_waitcnt lgkmcnt(0)
	buffer_inv sc1
	v_mad_u32_u24 v3, v2, v1, v1
	v_mov_b32_e32 v4, 0x2000
	s_mov_b32 s24, 0
.Lxbn_6:
	global_load_dword v5, v4, s[4:5] offset:1024 sc1
	s_waitcnt vmcnt(0)
	v_sub_u32_e32 v5, v5, v3
	v_cmp_gt_i32_e32 vcc, 0, v5
	s_cbranch_vccz .Lxbnd_6
	s_sleep 1
	s_add_u32 s24, s24, 1
	s_cmp_lt_u32 s24, 0x100000
	s_cbranch_scc1 .Lxbn_6

.LBB0_973:
	s_andn2_saveexec_b64 s[6:7], s[6:7]
	s_cbranch_execz .LBB0_991
	buffer_wbl2 sc1
	s_waitcnt vmcnt(0) lgkmcnt(0)
	v_mad_u32_u24 v3, v2, v1, v1
	v_mov_b32_e32 v4, 0x6400
	v_mov_b32_e32 v6, 1
	global_atomic_add v4, v6, s[48:49]
	v_add_u32_e32 v4, 0x100, v4
	global_atomic_add v4, v6, s[48:49]
	v_add_u32_e32 v4, 0x100, v4
	global_atomic_add v4, v6, s[48:49]
	v_add_u32_e32 v4, 0x100, v4
	global_atomic_add v4, v6, s[48:49]
	v_add_u32_e32 v4, 0x100, v4
	global_atomic_add v4, v6, s[48:49]
	v_add_u32_e32 v4, 0x100, v4
	global_atomic_add v4, v6, s[48:49]
	v_add_u32_e32 v4, 0x100, v4
	global_atomic_add v4, v6, s[48:49]
	v_add_u32_e32 v4, 0x100, v4
	global_atomic_add v4, v6, s[48:49]
	v_add_u32_e32 v4, 0x100, v4
	global_atomic_add v4, v6, s[48:49]
	v_add_u32_e32 v4, 0x100, v4
	global_atomic_add v4, v6, s[48:49]
	v_add_u32_e32 v4, 0x100, v4
	global_atomic_add v4, v6, s[48:49]
	v_add_u32_e32 v4, 0x100, v4
	global_atomic_add v4, v6, s[48:49]
	v_add_u32_e32 v4, 0x100, v4
	global_atomic_add v4, v6, s[48:49]
	v_add_u32_e32 v4, 0x100, v4
	global_atomic_add v4, v6, s[48:49]
	v_add_u32_e32 v4, 0x100, v4
	global_atomic_add v4, v6, s[48:49]
	v_add_u32_e32 v4, 0x100, v4
	global_atomic_add v4, v6, s[48:49]
	buffer_inv sc1
	v_mov_b32_e32 v4, 0x2000
	s_mov_b32 s24, 0

.Lxbld_6:
	s_waitcnt vmcnt(0)
.LBB0_991:
	s_or_b64 exec, exec, s[0:1]
	v_mov_b32_e32 v18, v0
	s_cmpk_gt_i32 s76, 0xff
	s_waitcnt lgkmcnt(0)
	s_barrier
	s_cbranch_scc1 .LBB0_1002
	v_and_b32_e32 v19, 63, v18
	v_readlane_b32 s12, v253, 18
	v_lshlrev_b32_e32 v21, 4, v19
	v_readlane_b32 s22, v253, 28
	v_readlane_b32 s23, v253, 29
	s_nop 4
	global_load_dwordx4 v[2:5], v21, s[22:23]
	global_load_dwordx4 v[6:9], v21, s[22:23] offset:1024
	global_load_dwordx4 v[10:13], v21, s[22:23] offset:2048
	global_load_dwordx4 v[14:17], v21, s[22:23] offset:3072
	v_mbcnt_lo_u32_b32 v25, -1, 0
	v_mbcnt_hi_u32_b32 v34, -1, v25
	v_and_b32_e32 v27, 64, v34
	v_xor_b32_e32 v25, 16, v34
	v_add_u32_e32 v29, 64, v27
	v_cmp_lt_i32_e32 vcc, v25, v29
	v_and_b32_e32 v20, 15, v18
	v_lshrrev_b32_e32 v22, 6, v18
	v_cndmask_b32_e32 v25, v34, v25, vcc
	v_lshlrev_b32_e32 v39, 2, v25
	v_xor_b32_e32 v25, 32, v34
	v_cmp_lt_i32_e32 vcc, v25, v29
	v_bfe_u32 v33, v18, 6, 1
	v_ashrrev_i32_e32 v1, 7, v18
	v_cndmask_b32_e32 v25, v34, v25, vcc
	v_lshlrev_b32_e32 v40, 2, v25
	v_and_b32_e32 v25, 0xffffff80, v18
	v_add_u32_e32 v25, 0, v25
	v_lshlrev_b32_e32 v31, 6, v33
	v_lshlrev_b32_e32 v32, 2, v20
	v_bitop3_b32 v22, v22, 1, v22 bitop3:0xc
	v_lshl_add_u32 v24, v1, 11, 0
	v_lshlrev_b32_e32 v30, 10, v33
	v_add3_u32 v42, v25, v31, v32
	v_lshlrev_b32_e32 v31, 10, v22
	v_lshrrev_b32_e32 v23, 2, v18
	v_add3_u32 v41, v24, v30, v21
	v_add3_u32 v43, v24, v31, v21
	v_lshlrev_b32_e32 v21, 6, v22
	v_and_b32_e32 v38, 12, v23
	v_add3_u32 v44, v25, v21, v32
	v_bfe_u32 v21, v18, 5, 1
	v_cmp_eq_u32_e64 s[4:5], v21, v33
	v_or_b32_e32 v21, v27, v38
	v_lshlrev_b32_e32 v45, 2, v21
	v_xor_b32_e32 v21, 1, v34
	v_cmp_lt_i32_e32 vcc, v21, v29
	v_mov_b32_e32 v23, 0
	v_lshlrev_b32_e32 v28, 12, v20
	v_cndmask_b32_e32 v21, v34, v21, vcc
	v_lshlrev_b32_e32 v46, 2, v21
	v_xor_b32_e32 v21, 2, v34
	v_cmp_lt_i32_e32 vcc, v21, v29
	v_lshlrev_b32_e32 v26, 2, v19
	v_cmp_gt_u32_e64 s[0:1], 16, v19
	v_cndmask_b32_e32 v21, v34, v21, vcc
	v_lshlrev_b32_e32 v47, 2, v21
	v_xor_b32_e32 v21, 4, v34
	v_cmp_lt_i32_e32 vcc, v21, v29
	v_lshlrev_b32_e32 v22, 3, v19
	v_readlane_b32 s6, v252, 9
	v_cndmask_b32_e32 v21, v34, v21, vcc
	v_lshlrev_b32_e32 v48, 2, v21
	v_xor_b32_e32 v21, 8, v34
	v_cmp_lt_i32_e32 vcc, v21, v29
	v_lshlrev_b32_e32 v19, 11, v33
	v_lshl_add_u64 v[24:25], s[84:85], 0, v[22:23]
	v_cndmask_b32_e32 v21, v34, v21, vcc
	v_lshlrev_b32_e32 v49, 2, v21
	v_and_b32_e32 v21, 48, v18
	v_mov_b32_e32 v27, v23
	v_readlane_b32 s7, v252, 10
	v_or3_b32 v22, v28, v19, v21
	v_lshrrev_b32_e32 v18, 1, v18
	v_lshl_add_u64 v[26:27], s[6:7], 0, v[26:27]
	v_lshl_add_u64 v[28:29], s[48:49], 0, v[22:23]
	s_mov_b64 s[6:7], 0x300100
	v_and_or_b32 v22, v18, 24, v30
	v_lshl_add_u64 v[28:29], v[28:29], 0, s[6:7]
	v_lshl_add_u64 v[18:19], s[48:49], 0, v[22:23]
	s_mov_b64 s[6:7], 0x800080
	v_lshl_add_u64 v[30:31], v[18:19], 0, s[6:7]
	v_lshlrev_b32_e32 v18, 4, v1
	v_lshl_add_u32 v18, s76, 6, v18
	v_readlane_b32 s13, v253, 19
	v_readlane_b32 s14, v253, 20
	v_readlane_b32 s15, v253, 21
	v_readlane_b32 s16, v253, 22
	v_readlane_b32 s17, v253, 23
	v_or_b32_e32 v32, v18, v20
	v_lshl_or_b32 v22, v33, 3, v18
	v_lshlrev_b32_e32 v18, 2, v34
	v_lshlrev_b32_e32 v19, 5, v33
	s_movk_i32 s6, 0x100
	s_lshl_b32 s10, s91, 2
	s_lshl_b32 s11, s76, 2
	v_or_b32_e32 v50, 4, v45
	v_or_b32_e32 v51, 8, v45
	v_or_b32_e32 v52, 12, v45
	s_lshl_b32 s12, s91, 6
	v_and_or_b32 v53, v18, s6, v19
	s_mov_b64 s[6:7], 0x200
	v_mov_b32_e32 v54, 0x358637bd
	s_mov_b32 s13, 0x800000
	s_mov_b32 s14, 0x3fb8aa3b
	s_mov_b32 s15, 0xc2ce8ed0
	s_mov_b32 s16, 0x42b17218
	v_lshlrev_b32_e32 v55, 2, v20
	v_mov_b32_e32 v56, -1
	s_mov_b32 s17, 0xc3e00000
	v_mov_b32_e32 v57, 0x7f800000
	v_mov_b32_e32 v58, 0x43e00000
	v_readlane_b32 s18, v253, 24
	v_readlane_b32 s19, v253, 25
	v_readlane_b32 s20, v253, 26
	v_readlane_b32 s21, v253, 27
	v_readlane_b32 s24, v253, 30
	v_readlane_b32 s25, v253, 31
	v_readlane_b32 s26, v253, 32
	v_readlane_b32 s27, v253, 33

.Lxbld_7:
	s_waitcnt vmcnt(0)
.LBB0_1094:
	s_or_b64 exec, exec, s[0:1]
	s_waitcnt lgkmcnt(0)
	s_barrier

.Lxbld_8:
	s_waitcnt vmcnt(0)
.LBB0_1380:
	s_or_b64 exec, exec, s[0:1]
	s_waitcnt lgkmcnt(0)
	s_barrier

.Lxbld_9:
	s_waitcnt vmcnt(0)
.LBB0_1449:
	s_or_b64 exec, exec, s[0:1]
	s_waitcnt lgkmcnt(0)
	s_barrier

.Lxbld_10:
	s_waitcnt vmcnt(0)
.LBB0_1517:
	s_or_b64 exec, exec, s[0:1]
	s_waitcnt lgkmcnt(0)
	s_barrier

.LBB0_1572:
	v_readlane_b32 s2, v253, 36
	s_lshl_b32 s2, s2, 8
	v_readlane_b32 s4, v253, 34
	v_readlane_b32 s5, v253, 35
	s_add_u32 s2, s4, s2
	s_addc_u32 s3, s5, 0
	v_mov_b32_e32 v3, 0x1000
	v_mov_b32_e32 v5, 1
	global_atomic_add v5, v3, v5, s[2:3] offset:1024 sc0
	v_cvt_f32_u32_e32 v3, v4
	v_sub_u32_e32 v6, 0, v4
	v_rcp_iflag_f32_e32 v3, v3
	s_nop 0
	v_mul_f32_e32 v3, 0x4f7ffffe, v3
	v_cvt_u32_f32_e32 v3, v3
	v_mul_lo_u32 v6, v6, v3
	v_mul_hi_u32 v6, v3, v6
	v_add_u32_e32 v3, v3, v6
	s_waitcnt vmcnt(0)
	v_mul_hi_u32 v3, v5, v3
	v_mul_lo_u32 v6, v3, v4
	v_sub_u32_e32 v6, v5, v6
	v_add_u32_e32 v7, 1, v3
	v_cmp_ge_u32_e32 vcc, v6, v4
	v_add_u32_e32 v5, 1, v5
	s_nop 0
	v_cndmask_b32_e32 v3, v3, v7, vcc
	v_sub_u32_e32 v7, v6, v4
	v_cndmask_b32_e32 v6, v6, v7, vcc
	v_add_u32_e32 v7, 1, v3
	v_cmp_ge_u32_e32 vcc, v6, v4
	s_nop 1
	v_cndmask_b32_e32 v3, v3, v7, vcc
	v_mul_lo_u32 v6, v4, v3
	v_add_u32_e32 v4, v6, v4
	v_cmp_ne_u32_e32 vcc, v5, v4
	s_and_saveexec_b64 s[4:5], vcc
	s_xor_b64 s[4:5], exec, s[4:5]
	s_cbranch_execz .LBB0_1586
	s_waitcnt lgkmcnt(0)
	buffer_inv sc1
	v_mad_u32_u24 v4, v3, v2, v2
	v_mov_b32_e32 v5, 0x2000
	s_mov_b32 s22, 0
.Lxbn_11:
	global_load_dword v6, v5, s[2:3] offset:1024 sc1
	s_waitcnt vmcnt(0)
	v_sub_u32_e32 v6, v6, v4
	v_cmp_gt_i32_e32 vcc, 0, v6
	s_cbranch_vccz .Lxbnd_11
	s_sleep 1
	s_add_u32 s22, s22, 1
	s_cmp_lt_u32 s22, 0x100000
	s_cbranch_scc1 .Lxbn_11

.LBB0_1586:
	s_andn2_saveexec_b64 s[4:5], s[4:5]
	s_cbranch_execz .LBB0_1604
	buffer_wbl2 sc1
	s_waitcnt vmcnt(0) lgkmcnt(0)
	v_mad_u32_u24 v4, v3, v2, v2
	v_mov_b32_e32 v5, 0x6400
	v_mov_b32_e32 v7, 1
	global_atomic_add v5, v7, s[48:49]
	v_add_u32_e32 v5, 0x100, v5
	global_atomic_add v5, v7, s[48:49]
	v_add_u32_e32 v5, 0x100, v5
	global_atomic_add v5, v7, s[48:49]
	v_add_u32_e32 v5, 0x100, v5
	global_atomic_add v5, v7, s[48:49]
	v_add_u32_e32 v5, 0x100, v5
	global_atomic_add v5, v7, s[48:49]
	v_add_u32_e32 v5, 0x100, v5
	global_atomic_add v5, v7, s[48:49]
	v_add_u32_e32 v5, 0x100, v5
	global_atomic_add v5, v7, s[48:49]
	v_add_u32_e32 v5, 0x100, v5
	global_atomic_add v5, v7, s[48:49]
	v_add_u32_e32 v5, 0x100, v5
	global_atomic_add v5, v7, s[48:49]
	v_add_u32_e32 v5, 0x100, v5
	global_atomic_add v5, v7, s[48:49]
	v_add_u32_e32 v5, 0x100, v5
	global_atomic_add v5, v7, s[48:49]
	v_add_u32_e32 v5, 0x100, v5
	global_atomic_add v5, v7, s[48:49]
	v_add_u32_e32 v5, 0x100, v5
	global_atomic_add v5, v7, s[48:49]
	v_add_u32_e32 v5, 0x100, v5
	global_atomic_add v5, v7, s[48:49]
	v_add_u32_e32 v5, 0x100, v5
	global_atomic_add v5, v7, s[48:49]
	v_add_u32_e32 v5, 0x100, v5
	global_atomic_add v5, v7, s[48:49]
	buffer_inv sc1
	v_mov_b32_e32 v5, 0x2000
	s_mov_b32 s22, 0

.Lxbld_11:
	s_waitcnt vmcnt(0)
.LBB0_1604:
	s_or_b64 exec, exec, s[0:1]
	s_waitcnt lgkmcnt(0)
	s_barrier

.Lxbld_12:
	s_waitcnt vmcnt(0)
.LBB0_1673:
	s_or_b64 exec, exec, s[0:1]
	s_waitcnt lgkmcnt(0)
	s_barrier

.LBB0_1790:
	v_readlane_b32 s4, v253, 36
	s_lshl_b32 s4, s4, 8
	v_readlane_b32 s6, v253, 34
	v_readlane_b32 s7, v253, 35
	s_add_u32 s4, s6, s4
	s_addc_u32 s5, s7, 0
	v_mov_b32_e32 v3, 0x1000
	v_mov_b32_e32 v5, 1
	global_atomic_add v5, v3, v5, s[4:5] offset:1024 sc0
	v_cvt_f32_u32_e32 v3, v4
	v_sub_u32_e32 v6, 0, v4
	v_rcp_iflag_f32_e32 v3, v3
	s_nop 0
	v_mul_f32_e32 v3, 0x4f7ffffe, v3
	v_cvt_u32_f32_e32 v3, v3
	v_mul_lo_u32 v6, v6, v3
	v_mul_hi_u32 v6, v3, v6
	v_add_u32_e32 v3, v3, v6
	s_waitcnt vmcnt(0)
	v_mul_hi_u32 v3, v5, v3
	v_mul_lo_u32 v6, v3, v4
	v_sub_u32_e32 v6, v5, v6
	v_add_u32_e32 v7, 1, v3
	v_cmp_ge_u32_e32 vcc, v6, v4
	v_add_u32_e32 v5, 1, v5
	s_nop 0
	v_cndmask_b32_e32 v3, v3, v7, vcc
	v_sub_u32_e32 v7, v6, v4
	v_cndmask_b32_e32 v6, v6, v7, vcc
	v_add_u32_e32 v7, 1, v3
	v_cmp_ge_u32_e32 vcc, v6, v4
	s_nop 1
	v_cndmask_b32_e32 v3, v3, v7, vcc
	v_mul_lo_u32 v6, v4, v3
	v_add_u32_e32 v4, v6, v4
	v_cmp_ne_u32_e32 vcc, v5, v4
	s_and_saveexec_b64 s[6:7], vcc
	s_xor_b64 s[6:7], exec, s[6:7]
	s_cbranch_execz .LBB0_1804
	s_waitcnt lgkmcnt(0)
	buffer_inv sc1
	v_mad_u32_u24 v4, v3, v2, v2
	v_mov_b32_e32 v5, 0x2000
	s_mov_b32 s26, 0
.Lxbn_13:
	global_load_dword v6, v5, s[4:5] offset:1024 sc1
	s_waitcnt vmcnt(0)
	v_sub_u32_e32 v6, v6, v4
	v_cmp_gt_i32_e32 vcc, 0, v6
	s_cbranch_vccz .Lxbnd_13
	s_sleep 1
	s_add_u32 s26, s26, 1
	s_cmp_lt_u32 s26, 0x100000
	s_cbranch_scc1 .Lxbn_13

.LBB0_1804:
	s_andn2_saveexec_b64 s[6:7], s[6:7]
	s_cbranch_execz .LBB0_1822
	buffer_wbl2 sc1
	s_waitcnt vmcnt(0) lgkmcnt(0)
	v_mad_u32_u24 v4, v3, v2, v2
	v_mov_b32_e32 v5, 0x6400
	v_mov_b32_e32 v7, 1
	global_atomic_add v5, v7, s[48:49]
	v_add_u32_e32 v5, 0x100, v5
	global_atomic_add v5, v7, s[48:49]
	v_add_u32_e32 v5, 0x100, v5
	global_atomic_add v5, v7, s[48:49]
	v_add_u32_e32 v5, 0x100, v5
	global_atomic_add v5, v7, s[48:49]
	v_add_u32_e32 v5, 0x100, v5
	global_atomic_add v5, v7, s[48:49]
	v_add_u32_e32 v5, 0x100, v5
	global_atomic_add v5, v7, s[48:49]
	v_add_u32_e32 v5, 0x100, v5
	global_atomic_add v5, v7, s[48:49]
	v_add_u32_e32 v5, 0x100, v5
	global_atomic_add v5, v7, s[48:49]
	v_add_u32_e32 v5, 0x100, v5
	global_atomic_add v5, v7, s[48:49]
	v_add_u32_e32 v5, 0x100, v5
	global_atomic_add v5, v7, s[48:49]
	v_add_u32_e32 v5, 0x100, v5
	global_atomic_add v5, v7, s[48:49]
	v_add_u32_e32 v5, 0x100, v5
	global_atomic_add v5, v7, s[48:49]
	v_add_u32_e32 v5, 0x100, v5
	global_atomic_add v5, v7, s[48:49]
	v_add_u32_e32 v5, 0x100, v5
	global_atomic_add v5, v7, s[48:49]
	v_add_u32_e32 v5, 0x100, v5
	global_atomic_add v5, v7, s[48:49]
	v_add_u32_e32 v5, 0x100, v5
	global_atomic_add v5, v7, s[48:49]
	buffer_inv sc1
	v_mov_b32_e32 v5, 0x2000
	s_mov_b32 s26, 0

.Lxbld_13:
	s_waitcnt vmcnt(0)
.LBB0_1822:
	s_or_b64 exec, exec, s[0:1]
	s_waitcnt lgkmcnt(0)
	s_barrier

.LBB0_1876:
	v_readlane_b32 s4, v253, 36
	s_lshl_b32 s4, s4, 8
	v_readlane_b32 s6, v253, 34
	v_readlane_b32 s7, v253, 35
	s_add_u32 s4, s6, s4
	s_addc_u32 s5, s7, 0
	v_mov_b32_e32 v3, 0x1000
	v_mov_b32_e32 v5, 1
	global_atomic_add v5, v3, v5, s[4:5] offset:1024 sc0
	v_cvt_f32_u32_e32 v3, v4
	v_sub_u32_e32 v6, 0, v4
	v_rcp_iflag_f32_e32 v3, v3
	s_nop 0
	v_mul_f32_e32 v3, 0x4f7ffffe, v3
	v_cvt_u32_f32_e32 v3, v3
	v_mul_lo_u32 v6, v6, v3
	v_mul_hi_u32 v6, v3, v6
	v_add_u32_e32 v3, v3, v6
	s_waitcnt vmcnt(0)
	v_mul_hi_u32 v3, v5, v3
	v_mul_lo_u32 v6, v3, v4
	v_sub_u32_e32 v6, v5, v6
	v_add_u32_e32 v7, 1, v3
	v_cmp_ge_u32_e32 vcc, v6, v4
	v_add_u32_e32 v5, 1, v5
	s_nop 0
	v_cndmask_b32_e32 v3, v3, v7, vcc
	v_sub_u32_e32 v7, v6, v4
	v_cndmask_b32_e32 v6, v6, v7, vcc
	v_add_u32_e32 v7, 1, v3
	v_cmp_ge_u32_e32 vcc, v6, v4
	s_nop 1
	v_cndmask_b32_e32 v3, v3, v7, vcc
	v_mul_lo_u32 v6, v4, v3
	v_add_u32_e32 v4, v6, v4
	v_cmp_ne_u32_e32 vcc, v5, v4
	s_and_saveexec_b64 s[6:7], vcc
	s_xor_b64 s[6:7], exec, s[6:7]
	s_cbranch_execz .LBB0_1890
	s_waitcnt lgkmcnt(0)
	buffer_inv sc1
	v_mad_u32_u24 v4, v3, v2, v2
	v_mov_b32_e32 v5, 0x2000
	s_mov_b32 s24, 0
.Lxbn_14:
	global_load_dword v6, v5, s[4:5] offset:1024 sc1
	s_waitcnt vmcnt(0)
	v_sub_u32_e32 v6, v6, v4
	v_cmp_gt_i32_e32 vcc, 0, v6
	s_cbranch_vccz .Lxbnd_14
	s_sleep 1
	s_add_u32 s24, s24, 1
	s_cmp_lt_u32 s24, 0x100000
	s_cbranch_scc1 .Lxbn_14

.LBB0_1890:
	s_andn2_saveexec_b64 s[6:7], s[6:7]
	s_cbranch_execz .LBB0_1908
	buffer_wbl2 sc1
	s_waitcnt vmcnt(0) lgkmcnt(0)
	v_mad_u32_u24 v4, v3, v2, v2
	v_mov_b32_e32 v5, 0x6400
	v_mov_b32_e32 v7, 1
	global_atomic_add v5, v7, s[48:49]
	v_add_u32_e32 v5, 0x100, v5
	global_atomic_add v5, v7, s[48:49]
	v_add_u32_e32 v5, 0x100, v5
	global_atomic_add v5, v7, s[48:49]
	v_add_u32_e32 v5, 0x100, v5
	global_atomic_add v5, v7, s[48:49]
	v_add_u32_e32 v5, 0x100, v5
	global_atomic_add v5, v7, s[48:49]
	v_add_u32_e32 v5, 0x100, v5
	global_atomic_add v5, v7, s[48:49]
	v_add_u32_e32 v5, 0x100, v5
	global_atomic_add v5, v7, s[48:49]
	v_add_u32_e32 v5, 0x100, v5
	global_atomic_add v5, v7, s[48:49]
	v_add_u32_e32 v5, 0x100, v5
	global_atomic_add v5, v7, s[48:49]
	v_add_u32_e32 v5, 0x100, v5
	global_atomic_add v5, v7, s[48:49]
	v_add_u32_e32 v5, 0x100, v5
	global_atomic_add v5, v7, s[48:49]
	v_add_u32_e32 v5, 0x100, v5
	global_atomic_add v5, v7, s[48:49]
	v_add_u32_e32 v5, 0x100, v5
	global_atomic_add v5, v7, s[48:49]
	v_add_u32_e32 v5, 0x100, v5
	global_atomic_add v5, v7, s[48:49]
	v_add_u32_e32 v5, 0x100, v5
	global_atomic_add v5, v7, s[48:49]
	v_add_u32_e32 v5, 0x100, v5
	global_atomic_add v5, v7, s[48:49]
	buffer_inv sc1
	v_mov_b32_e32 v5, 0x2000
	s_mov_b32 s24, 0

.Lxbld_14:
	s_waitcnt vmcnt(0)
.LBB0_1908:
	s_or_b64 exec, exec, s[0:1]
	s_waitcnt lgkmcnt(0)
	s_barrier

.Lxbld_15:
	s_waitcnt vmcnt(0)
.LBB0_1976:
	s_or_b64 exec, exec, s[0:1]
	s_waitcnt lgkmcnt(0)
	s_barrier

.Lxbld_16:
	s_waitcnt vmcnt(0)
.LBB0_2033:
	s_or_b64 exec, exec, s[0:1]
	s_waitcnt lgkmcnt(0)
	s_barrier

.Lxbld_17:
	s_waitcnt vmcnt(0)
.LBB0_2127:
	s_or_b64 exec, exec, s[0:1]
	s_waitcnt lgkmcnt(0)
	s_barrier

.Lxbld_18:
	s_waitcnt vmcnt(0)
.LBB0_2195:
	s_or_b64 exec, exec, s[0:1]
	s_waitcnt lgkmcnt(0)
	s_barrier

.Lxbld_19:
	s_waitcnt vmcnt(0)
.LBB0_2271:
	s_or_b64 exec, exec, s[0:1]
	v_readlane_b32 s0, v253, 0
	v_mov_b32_e32 v18, v0
	s_cmpk_gt_i32 s0, 0xff
	s_waitcnt lgkmcnt(0)
	s_barrier
	v_readlane_b32 s1, v253, 1
	s_cbranch_scc1 .LBB0_2282
	v_readlane_b32 s4, v253, 18
	v_readlane_b32 s10, v253, 24
	v_readlane_b32 s11, v253, 25
	v_readlane_b32 s14, v253, 28
	v_readlane_b32 s15, v253, 29
	s_mov_b64 s[10:11], s[14:15]
	v_and_b32_e32 v19, 63, v18
	s_add_u32 s0, s10, 0x1000
	v_lshlrev_b32_e32 v21, 4, v19
	s_addc_u32 s1, s11, 0
	v_or_b32_e32 v10, 0x400, v21
	v_or_b32_e32 v20, 0x800, v21
	global_load_dwordx4 v[2:5], v21, s[0:1]
	global_load_dwordx4 v[6:9], v10, s[0:1]
	v_or_b32_e32 v22, 0xc00, v21
	global_load_dwordx4 v[10:13], v20, s[0:1]
	global_load_dwordx4 v[14:17], v22, s[0:1]
	v_mbcnt_lo_u32_b32 v25, -1, 0
	v_mbcnt_hi_u32_b32 v34, -1, v25
	v_and_b32_e32 v27, 64, v34
	v_xor_b32_e32 v25, 16, v34
	v_add_u32_e32 v29, 64, v27
	v_cmp_lt_i32_e32 vcc, v25, v29
	v_and_b32_e32 v20, 15, v18
	v_lshrrev_b32_e32 v22, 6, v18
	v_cndmask_b32_e32 v25, v34, v25, vcc
	v_lshlrev_b32_e32 v39, 2, v25
	v_xor_b32_e32 v25, 32, v34
	v_cmp_lt_i32_e32 vcc, v25, v29
	v_bfe_u32 v33, v18, 6, 1
	v_ashrrev_i32_e32 v1, 7, v18
	v_cndmask_b32_e32 v25, v34, v25, vcc
	v_lshlrev_b32_e32 v40, 2, v25
	v_and_b32_e32 v25, 0xffffff80, v18
	v_add_u32_e32 v25, 0, v25
	v_lshlrev_b32_e32 v31, 6, v33
	v_lshlrev_b32_e32 v32, 2, v20
	v_bitop3_b32 v22, v22, 1, v22 bitop3:0xc
	v_lshl_add_u32 v24, v1, 11, 0
	v_lshlrev_b32_e32 v30, 10, v33
	v_add3_u32 v42, v25, v31, v32
	v_lshlrev_b32_e32 v31, 10, v22
	v_lshrrev_b32_e32 v23, 2, v18
	v_add3_u32 v41, v24, v30, v21
	v_add3_u32 v43, v24, v31, v21
	v_lshlrev_b32_e32 v21, 6, v22
	v_readlane_b32 s5, v253, 19
	v_and_b32_e32 v38, 12, v23
	v_add3_u32 v44, v25, v21, v32
	v_bfe_u32 v21, v18, 5, 1
	v_cmp_eq_u32_e64 s[4:5], v21, v33
	v_or_b32_e32 v21, v27, v38
	v_lshlrev_b32_e32 v45, 2, v21
	v_xor_b32_e32 v21, 1, v34
	v_cmp_lt_i32_e32 vcc, v21, v29
	v_readlane_b32 s0, v253, 0
	v_readlane_b32 s8, v253, 22
	v_cndmask_b32_e32 v21, v34, v21, vcc
	v_lshlrev_b32_e32 v46, 2, v21
	v_xor_b32_e32 v21, 2, v34
	v_cmp_lt_i32_e32 vcc, v21, v29
	v_readlane_b32 s1, v253, 1
	s_mov_b32 s8, s0
	v_cndmask_b32_e32 v21, v34, v21, vcc
	v_lshlrev_b32_e32 v47, 2, v21
	v_xor_b32_e32 v21, 4, v34
	v_cmp_lt_i32_e32 vcc, v21, v29
	s_lshl_b32 s11, s0, 2
	v_mov_b32_e32 v23, 0
	v_cndmask_b32_e32 v21, v34, v21, vcc
	v_lshlrev_b32_e32 v48, 2, v21
	v_xor_b32_e32 v21, 8, v34
	v_cmp_lt_i32_e32 vcc, v21, v29
	v_lshlrev_b32_e32 v28, 12, v20
	v_lshlrev_b32_e32 v26, 2, v19
	v_cndmask_b32_e32 v21, v34, v21, vcc
	v_cmp_gt_u32_e64 s[0:1], 16, v19
	v_lshlrev_b32_e32 v49, 2, v21
	v_lshlrev_b32_e32 v22, 3, v19
	v_lshlrev_b32_e32 v19, 11, v33
	v_and_b32_e32 v21, 48, v18
	v_readlane_b32 s6, v253, 20
	v_readlane_b32 s7, v253, 21
	v_lshl_add_u64 v[24:25], s[84:85], 0, v[22:23]
	v_or3_b32 v22, v28, v19, v21
	v_lshrrev_b32_e32 v18, 1, v18
	v_lshl_add_u64 v[28:29], s[48:49], 0, v[22:23]
	s_mov_b64 s[6:7], 0x310100
	v_and_or_b32 v22, v18, 24, v30
	v_lshl_add_u64 v[28:29], v[28:29], 0, s[6:7]
	v_lshl_add_u64 v[18:19], s[48:49], 0, v[22:23]
	s_mov_b64 s[6:7], 0x800080
	v_lshl_add_u64 v[30:31], v[18:19], 0, s[6:7]
	v_lshlrev_b32_e32 v18, 4, v1
	v_lshl_add_u32 v18, s8, 6, v18
	v_readlane_b32 s12, v253, 26
	v_readlane_b32 s13, v253, 27
	v_readlane_b32 s16, v253, 30
	v_readlane_b32 s17, v253, 31
	v_mov_b32_e32 v27, v23
	v_or_b32_e32 v32, v18, v20
	v_lshl_or_b32 v22, v33, 3, v18
	v_lshlrev_b32_e32 v18, 2, v34
	v_lshlrev_b32_e32 v19, 5, v33
	s_movk_i32 s6, 0x100
	s_lshl_b32 s10, s91, 2
	v_or_b32_e32 v50, 4, v45
	v_or_b32_e32 v51, 8, v45
	v_or_b32_e32 v52, 12, v45
	v_lshl_add_u64 v[26:27], s[82:83], 0, v[26:27]
	s_lshl_b32 s12, s91, 6
	v_and_or_b32 v53, v18, s6, v19
	s_mov_b64 s[6:7], 0x200
	v_mov_b32_e32 v54, 0x358637bd
	s_mov_b32 s13, 0x800000
	s_mov_b32 s14, 0x3fb8aa3b
	s_mov_b32 s15, 0xc2ce8ed0
	s_mov_b32 s16, 0x42b17218
	v_lshlrev_b32_e32 v55, 2, v20
	v_mov_b32_e32 v56, -1
	s_mov_b32 s17, 0xc3e00000
	v_mov_b32_e32 v57, 0x7f800000
	v_mov_b32_e32 v58, 0x43e00000
	v_readlane_b32 s9, v253, 23
	v_readlane_b32 s18, v253, 32
	v_readlane_b32 s19, v253, 33

.Lxbld_20:
	s_waitcnt vmcnt(0)
.LBB0_2374:
	s_or_b64 exec, exec, s[0:1]
	s_waitcnt lgkmcnt(0)
	s_barrier

.Lxbld_21:
	s_waitcnt vmcnt(0)
.LBB0_2641:
	s_or_b64 exec, exec, s[0:1]
	s_waitcnt lgkmcnt(0)
	s_barrier

.Lxbld_22:
	s_waitcnt vmcnt(0)
.LBB0_2709:
	s_or_b64 exec, exec, s[0:1]
	s_waitcnt lgkmcnt(0)
	s_barrier

.Lxbld_23:
	s_waitcnt vmcnt(0)
.LBB0_2777:
	s_or_b64 exec, exec, s[0:1]
	s_waitcnt lgkmcnt(0)
	s_barrier
